# stack12
# speedup vs baseline: 1.0036x; 1.0036x over previous
.LBB3_21:
	s_or_b64 exec, exec, s[26:27]
	global_load_dwordx4 v[58:61], v[106:107], off
	global_load_dwordx4 v[62:65], v[108:109], off
	global_load_dwordx4 v[66:69], v[110:111], off
	global_load_dwordx4 v[70:73], v[112:113], off
	v_pk_mul_f32 v[182:183], v[6:7], v[164:165] op_sel_hi:[1,0] neg_lo:[0,1] neg_hi:[0,1]
	v_pk_mul_f32 v[184:185], v[8:9], v[164:165] op_sel_hi:[1,0] neg_lo:[0,1] neg_hi:[0,1]
	v_pk_mul_f32 v[186:187], v[2:3], v[164:165] op_sel_hi:[1,0] neg_lo:[0,1] neg_hi:[0,1]
	v_pk_mul_f32 v[188:189], v[4:5], v[164:165] op_sel_hi:[1,0] neg_lo:[0,1] neg_hi:[0,1]
	v_pk_mul_f32 v[198:199], v[14:15], v[164:165] op_sel_hi:[1,0] neg_lo:[0,1] neg_hi:[0,1]
	v_pk_mul_f32 v[200:201], v[16:17], v[164:165] op_sel_hi:[1,0] neg_lo:[0,1] neg_hi:[0,1]
	v_pk_mul_f32 v[202:203], v[10:11], v[164:165] op_sel_hi:[1,0] neg_lo:[0,1] neg_hi:[0,1]
	v_pk_mul_f32 v[204:205], v[12:13], v[164:165] op_sel_hi:[1,0] neg_lo:[0,1] neg_hi:[0,1]
	v_pk_mul_f32 v[214:215], v[22:23], v[164:165] op_sel_hi:[1,0] neg_lo:[0,1] neg_hi:[0,1]
	v_pk_mul_f32 v[216:217], v[24:25], v[164:165] op_sel_hi:[1,0] neg_lo:[0,1] neg_hi:[0,1]
	v_pk_mul_f32 v[218:219], v[18:19], v[164:165] op_sel_hi:[1,0] neg_lo:[0,1] neg_hi:[0,1]
	v_pk_mul_f32 v[220:221], v[20:21], v[164:165] op_sel_hi:[1,0] neg_lo:[0,1] neg_hi:[0,1]
	v_pk_mul_f32 v[222:223], v[30:31], v[164:165] op_sel_hi:[1,0] neg_lo:[0,1] neg_hi:[0,1]
	v_pk_mul_f32 v[224:225], v[32:33], v[164:165] op_sel_hi:[1,0] neg_lo:[0,1] neg_hi:[0,1]
	v_pk_mul_f32 v[226:227], v[26:27], v[164:165] op_sel_hi:[1,0] neg_lo:[0,1] neg_hi:[0,1]
	v_pk_mul_f32 v[228:229], v[28:29], v[164:165] op_sel_hi:[1,0] neg_lo:[0,1] neg_hi:[0,1]
	s_andn2_b64 vcc, exec, s[10:11]
	s_mov_b64 s[24:25], -1
	s_cbranch_vccnz .LBB3_23
	s_mov_b64 s[24:25], 0

.LBB3_36:
	s_setprio 0
	global_load_dwordx4 v[58:61], v[114:115], off
	global_load_dwordx4 v[62:65], v[116:117], off
	global_load_dwordx4 v[66:69], v[118:119], off
	global_load_dwordx4 v[70:73], v[120:121], off
	ds_read_u16 v82, v233
	s_waitcnt lgkmcnt(1)
	v_bfe_u32 v76, v231, 23, 8
	s_cmp_eq_u32 s34, 1
	v_max_u32_e32 v76, 11, v76
	s_cselect_b64 s[24:25], -1, 0
	v_lshlrev_b32_e32 v240, 23, v76
	v_cndmask_b32_e64 v76, 2.0, 1.0, s[24:25]
	s_lshl_b32 s8, s34, 16
	v_mul_f32_e32 v230, v76, v230
	s_and_b32 s67, s8, 0x10000
	v_sub_u32_e32 v164, 0x84000000, v240
	v_pk_fma_f32 v[182:183], v[230:231], v[182:183], v[212:213] op_sel_hi:[0,1,1] neg_lo:[0,0,1] neg_hi:[0,0,1]
	v_pk_fma_f32 v[184:185], v[230:231], v[184:185], v[210:211] op_sel_hi:[0,1,1] neg_lo:[0,0,1] neg_hi:[0,0,1]
	v_pk_fma_f32 v[186:187], v[230:231], v[186:187], v[208:209] op_sel_hi:[0,1,1] neg_lo:[0,0,1] neg_hi:[0,0,1]
	v_pk_fma_f32 v[188:189], v[230:231], v[188:189], v[206:207] op_sel_hi:[0,1,1] neg_lo:[0,0,1] neg_hi:[0,0,1]
	v_fma_mixlo_f16 v78, v182, v164, 0 op_sel_hi:[0,0,0]
	v_fma_mixlo_f16 v79, v184, v164, 0 op_sel_hi:[0,0,0]
	v_fma_mixlo_f16 v80, v186, v164, 0 op_sel_hi:[0,0,0]
	v_fma_mixlo_f16 v81, v188, v164, 0 op_sel_hi:[0,0,0]
	s_waitcnt lgkmcnt(0)
	v_lshl_add_u32 v82, v82, 4, s67
	v_fma_mixhi_f16 v78, v183, v164, 0 op_sel_hi:[0,0,0]
	v_fma_mixhi_f16 v79, v185, v164, 0 op_sel_hi:[0,0,0]
	v_fma_mixhi_f16 v80, v187, v164, 0 op_sel_hi:[0,0,0]
	v_fma_mixhi_f16 v81, v189, v164, 0 op_sel_hi:[0,0,0]
	ds_write_b128 v82, v[78:81]
	ds_read_u16 v82, v233 offset:1024
	v_pk_fma_f32 v[198:199], v[230:231], v[198:199], v[196:197] op_sel_hi:[0,1,1] neg_lo:[0,0,1] neg_hi:[0,0,1]
	v_pk_fma_f32 v[200:201], v[230:231], v[200:201], v[194:195] op_sel_hi:[0,1,1] neg_lo:[0,0,1] neg_hi:[0,0,1]
	v_pk_fma_f32 v[202:203], v[230:231], v[202:203], v[192:193] op_sel_hi:[0,1,1] neg_lo:[0,0,1] neg_hi:[0,0,1]
	v_pk_fma_f32 v[204:205], v[230:231], v[204:205], v[190:191] op_sel_hi:[0,1,1] neg_lo:[0,0,1] neg_hi:[0,0,1]
	v_fma_mixlo_f16 v78, v198, v164, 0 op_sel_hi:[0,0,0]
	v_fma_mixlo_f16 v79, v200, v164, 0 op_sel_hi:[0,0,0]
	v_fma_mixlo_f16 v80, v202, v164, 0 op_sel_hi:[0,0,0]
	v_fma_mixlo_f16 v81, v204, v164, 0 op_sel_hi:[0,0,0]
	s_waitcnt lgkmcnt(0)
	v_lshl_add_u32 v82, v82, 4, s67
	v_fma_mixhi_f16 v78, v199, v164, 0 op_sel_hi:[0,0,0]
	v_fma_mixhi_f16 v79, v201, v164, 0 op_sel_hi:[0,0,0]
	v_fma_mixhi_f16 v80, v203, v164, 0 op_sel_hi:[0,0,0]
	v_fma_mixhi_f16 v81, v205, v164, 0 op_sel_hi:[0,0,0]
	ds_write_b128 v82, v[78:81]
	ds_read_u16 v82, v233 offset:2048
	v_pk_fma_f32 v[214:215], v[230:231], v[214:215], v[180:181] op_sel_hi:[0,1,1] neg_lo:[0,0,1] neg_hi:[0,0,1]
	v_pk_fma_f32 v[216:217], v[230:231], v[216:217], v[178:179] op_sel_hi:[0,1,1] neg_lo:[0,0,1] neg_hi:[0,0,1]
	v_pk_fma_f32 v[218:219], v[230:231], v[218:219], v[176:177] op_sel_hi:[0,1,1] neg_lo:[0,0,1] neg_hi:[0,0,1]
	v_pk_fma_f32 v[220:221], v[230:231], v[220:221], v[174:175] op_sel_hi:[0,1,1] neg_lo:[0,0,1] neg_hi:[0,0,1]
	v_fma_mixlo_f16 v78, v214, v164, 0 op_sel_hi:[0,0,0]
	v_fma_mixlo_f16 v79, v216, v164, 0 op_sel_hi:[0,0,0]
	v_fma_mixlo_f16 v80, v218, v164, 0 op_sel_hi:[0,0,0]
	v_fma_mixlo_f16 v81, v220, v164, 0 op_sel_hi:[0,0,0]
	s_waitcnt lgkmcnt(0)
	v_lshl_add_u32 v82, v82, 4, s67
	v_fma_mixhi_f16 v78, v215, v164, 0 op_sel_hi:[0,0,0]
	v_fma_mixhi_f16 v79, v217, v164, 0 op_sel_hi:[0,0,0]
	v_fma_mixhi_f16 v80, v219, v164, 0 op_sel_hi:[0,0,0]
	v_fma_mixhi_f16 v81, v221, v164, 0 op_sel_hi:[0,0,0]
	ds_write_b128 v82, v[78:81]
	ds_read_u16 v82, v233 offset:3072
	v_pk_fma_f32 v[222:223], v[230:231], v[222:223], v[172:173] op_sel_hi:[0,1,1] neg_lo:[0,0,1] neg_hi:[0,0,1]
	v_pk_fma_f32 v[224:225], v[230:231], v[224:225], v[170:171] op_sel_hi:[0,1,1] neg_lo:[0,0,1] neg_hi:[0,0,1]
	v_pk_fma_f32 v[226:227], v[230:231], v[226:227], v[168:169] op_sel_hi:[0,1,1] neg_lo:[0,0,1] neg_hi:[0,0,1]
	v_pk_fma_f32 v[228:229], v[230:231], v[228:229], v[166:167] op_sel_hi:[0,1,1] neg_lo:[0,0,1] neg_hi:[0,0,1]
	v_fma_mixlo_f16 v78, v222, v164, 0 op_sel_hi:[0,0,0]
	v_fma_mixlo_f16 v79, v224, v164, 0 op_sel_hi:[0,0,0]
	v_fma_mixlo_f16 v80, v226, v164, 0 op_sel_hi:[0,0,0]
	v_fma_mixlo_f16 v81, v228, v164, 0 op_sel_hi:[0,0,0]
	s_waitcnt lgkmcnt(0)
	v_lshl_add_u32 v82, v82, 4, s67
	v_fma_mixhi_f16 v78, v223, v164, 0 op_sel_hi:[0,0,0]
	v_fma_mixhi_f16 v79, v225, v164, 0 op_sel_hi:[0,0,0]
	v_fma_mixhi_f16 v80, v227, v164, 0 op_sel_hi:[0,0,0]
	v_fma_mixhi_f16 v81, v229, v164, 0 op_sel_hi:[0,0,0]
	v_pk_mul_f32 v[206:207], v[38:39], v[74:75]
	v_pk_mul_f32 v[208:209], v[40:41], v[74:75]
	v_pk_mul_f32 v[210:211], v[34:35], v[74:75]
	v_pk_mul_f32 v[212:213], v[36:37], v[74:75]
	v_pk_mul_f32 v[190:191], v[46:47], v[74:75]
	v_pk_mul_f32 v[192:193], v[48:49], v[74:75]
	v_pk_mul_f32 v[194:195], v[42:43], v[74:75]
	v_pk_mul_f32 v[196:197], v[44:45], v[74:75]
	v_pk_mul_f32 v[174:175], v[54:55], v[74:75]
	v_pk_mul_f32 v[176:177], v[56:57], v[74:75]
	v_pk_mul_f32 v[178:179], v[50:51], v[74:75]
	v_pk_mul_f32 v[180:181], v[52:53], v[74:75]
	v_pk_mul_f32 v[166:167], v[124:125], v[74:75]
	v_pk_mul_f32 v[168:169], v[128:129], v[74:75]
	v_pk_mul_f32 v[170:171], v[126:127], v[74:75]
	v_pk_mul_f32 v[172:173], v[130:131], v[74:75]
	s_andn2_b64 vcc, exec, s[12:13]
	s_mov_b64 s[24:25], -1
	ds_write_b128 v82, v[78:81]
	s_cbranch_vccnz .LBB3_38
	s_mov_b64 s[24:25], 0
